# S3 fwd head-norm reduction via permlane swaps; retention decay load + expf chain moved behind the state/chunk load issue
# baseline (speedup 1.0000x reference)
.LBB0_702:
	s_lshl_b32 s20, s75, 2
	s_or_b32 s78, s20, s59
	s_lshl_b64 s[20:21], s[78:79], 2
	v_readlane_b32 s42, v241, 59
	s_add_u32 s20, s42, s20
	v_readlane_b32 s42, v241, 61
	s_addc_u32 s21, s42, s21
	global_load_dword v244, v65, s[20:21]
	s_mov_b32 s20, 0xc2ce8ed0
	s_mov_b32 s43, s75
	v_readlane_b32 s52, v241, 55
	s_mov_b32 s53, s79
	s_mov_b32 s84, 0
	v_readlane_b32 s72, v241, 51
	s_mov_b32 s83, 1
	s_mov_b32 s20, 0x42b17218
	s_add_i32 s20, s75, s76
	s_mul_hi_i32 s21, s20, 0x41
	v_add_co_u32_e64 v8, s[48:49], s43, -1
	s_nop 0
	v_readfirstlane_b32 s75, v8
	v_cndmask_b32_e64 v8, 0, 1, s[48:49]
	v_readlane_b32 s48, v242, 58
	v_mov_b32_e32 v9, s79
	v_readlane_b32 s49, v242, 59
	s_mulk_i32 s20, 0x41
	s_cmp_lg_u32 s43, 0
	v_lshl_add_u64 v[8:9], v[8:9], 0, s[48:49]
	v_lshl_add_u64 v[8:9], v[8:9], 0, s[20:21]
	v_readlane_b32 s20, v242, 60
	v_lshlrev_b64 v[8:9], 15, v[8:9]
	v_readlane_b32 s21, v242, 61
	s_cselect_b64 s[48:49], -1, 0
	s_cmp_eq_u32 s43, 0
	v_lshl_add_u64 v[8:9], s[20:21], 0, v[8:9]
	v_lshl_add_u64 v[10:11], v[8:9], 0, v[68:69]
	global_load_dwordx2 v[88:89], v[10:11], off nt
	v_lshl_add_u64 v[10:11], v[8:9], 0, v[70:71]
	global_load_dwordx2 v[92:93], v[10:11], off nt
	v_lshl_add_u64 v[10:11], v[8:9], 0, v[72:73]
	global_load_dwordx2 v[96:97], v[10:11], off nt
	v_lshl_add_u64 v[10:11], v[8:9], 0, v[74:75]
	global_load_dwordx2 v[100:101], v[10:11], off nt
	v_lshl_add_u64 v[10:11], v[8:9], 0, v[76:77]
	global_load_dwordx2 v[104:105], v[10:11], off nt
	v_lshl_add_u64 v[10:11], v[8:9], 0, v[78:79]
	global_load_dwordx2 v[108:109], v[10:11], off nt
	v_lshl_add_u64 v[10:11], v[8:9], 0, v[80:81]
	global_load_dwordx2 v[112:113], v[10:11], off nt
	v_lshl_add_u64 v[10:11], v[8:9], 0, v[82:83]
	global_load_dwordx2 v[116:117], v[10:11], off nt
	s_cselect_b64 s[20:21], -1, 0
	s_and_b64 s[50:51], s[20:21], exec
	v_readlane_b32 s50, v241, 45
	v_readlane_b32 s51, v241, 19
	s_cselect_b32 s77, s50, s51
	v_readlane_b32 s50, v241, 23
	v_readlane_b32 s51, v241, 21
	s_cselect_b32 s88, s50, s51
	v_readlane_b32 s50, v241, 27
	v_readlane_b32 s51, v241, 25
	s_cselect_b32 s85, s50, s51
	v_readlane_b32 s50, v241, 31
	v_readlane_b32 s51, v241, 29
	s_cselect_b32 s92, s50, s51
	v_readlane_b32 s50, v241, 35
	v_readlane_b32 s51, v241, 33
	s_cselect_b32 s89, s50, s51
	v_readlane_b32 s50, v241, 39
	v_readlane_b32 s51, v241, 37
	s_cselect_b32 s96, s50, s51
	v_readlane_b32 s50, v241, 43
	v_readlane_b32 s51, v241, 41
	s_cselect_b32 s42, 0, 0x1c0
	s_cselect_b32 s93, s50, s51
	v_readlane_b32 s50, v241, 49
	v_readlane_b32 s51, v241, 47
	s_cselect_b32 s58, s50, s51
	s_add_i32 s42, s42, s74
	s_add_i32 s50, s42, s77
	s_lshl_b32 s78, s73, 1
	s_lshl_b32 s52, s52, 1
	s_add_i32 s54, s42, s88
	v_mad_i64_i32 v[8:9], s[50:51], s50, v205, v[66:67]
	v_lshl_add_u64 v[10:11], v[8:9], 0, s[78:79]
	s_lshl_b32 s50, s71, 1
	s_mov_b32 s51, s79
	global_load_dword v140, v[10:11], off
	v_lshl_add_u64 v[10:11], v[8:9], 0, s[50:51]
	v_lshl_add_u64 v[8:9], v[8:9], 0, s[52:53]
	global_load_dword v141, v[10:11], off
	global_load_dword v142, v[8:9], off
	v_mad_i64_i32 v[8:9], s[54:55], s54, v205, v[66:67]
	v_lshl_add_u64 v[10:11], v[8:9], 0, s[78:79]
	global_load_dword v143, v[10:11], off
	v_lshl_add_u64 v[10:11], v[8:9], 0, s[50:51]
	v_lshl_add_u64 v[8:9], v[8:9], 0, s[52:53]
	s_add_i32 s54, s42, s85
	global_load_dword v144, v[10:11], off
	global_load_dword v145, v[8:9], off
	v_mad_i64_i32 v[8:9], s[54:55], s54, v205, v[66:67]
	v_lshl_add_u64 v[10:11], v[8:9], 0, s[78:79]
	global_load_dword v166, v[10:11], off
	v_lshl_add_u64 v[10:11], v[8:9], 0, s[50:51]
	v_lshl_add_u64 v[8:9], v[8:9], 0, s[52:53]
	s_add_i32 s54, s42, s92
	global_load_dword v167, v[10:11], off
	global_load_dword v168, v[8:9], off
	v_mad_i64_i32 v[8:9], s[54:55], s54, v205, v[66:67]
	v_lshl_add_u64 v[10:11], v[8:9], 0, s[78:79]
	global_load_dword v169, v[10:11], off
	v_lshl_add_u64 v[10:11], v[8:9], 0, s[50:51]
	v_lshl_add_u64 v[8:9], v[8:9], 0, s[52:53]
	s_add_i32 s54, s42, s89
	global_load_dword v170, v[10:11], off
	global_load_dword v171, v[8:9], off
	v_mad_i64_i32 v[8:9], s[54:55], s54, v205, v[66:67]
	v_lshl_add_u64 v[10:11], v[8:9], 0, s[78:79]
	global_load_dword v172, v[10:11], off
	v_lshl_add_u64 v[10:11], v[8:9], 0, s[50:51]
	v_lshl_add_u64 v[8:9], v[8:9], 0, s[52:53]
	s_add_i32 s54, s42, s96
	global_load_dword v173, v[10:11], off
	global_load_dword v174, v[8:9], off
	v_mad_i64_i32 v[8:9], s[54:55], s54, v205, v[66:67]
	v_lshl_add_u64 v[10:11], v[8:9], 0, s[78:79]
	global_load_dword v175, v[10:11], off
	v_lshl_add_u64 v[10:11], v[8:9], 0, s[50:51]
	v_lshl_add_u64 v[8:9], v[8:9], 0, s[52:53]
	s_add_i32 s54, s42, s93
	global_load_dword v176, v[10:11], off
	global_load_dword v177, v[8:9], off
	v_mad_i64_i32 v[8:9], s[54:55], s54, v205, v[66:67]
	v_lshl_add_u64 v[10:11], v[8:9], 0, s[78:79]
	global_load_dword v178, v[10:11], off
	v_lshl_add_u64 v[10:11], v[8:9], 0, s[50:51]
	v_lshl_add_u64 v[8:9], v[8:9], 0, s[52:53]
	s_add_i32 s42, s42, s58
	global_load_dword v179, v[10:11], off
	global_load_dword v180, v[8:9], off
	v_mad_i64_i32 v[8:9], s[54:55], s42, v205, v[66:67]
	v_lshl_add_u64 v[10:11], v[8:9], 0, s[78:79]
	global_load_dword v181, v[10:11], off
	v_lshl_add_u64 v[10:11], v[8:9], 0, s[50:51]
	v_lshl_add_u64 v[8:9], v[8:9], 0, s[52:53]
	global_load_dword v182, v[10:11], off
	global_load_dword v191, v[8:9], off
	s_waitcnt vmcnt(31)
	v_lshlrev_b32_e32 v86, 16, v88
	v_and_b32_e32 v87, 0xffff0000, v88
	v_lshlrev_b32_e32 v88, 16, v89
	v_and_b32_e32 v89, 0xffff0000, v89
	s_waitcnt vmcnt(30)
	v_lshlrev_b32_e32 v90, 16, v92
	v_and_b32_e32 v91, 0xffff0000, v92
	v_lshlrev_b32_e32 v92, 16, v93
	v_and_b32_e32 v93, 0xffff0000, v93
	s_waitcnt vmcnt(29)
	v_lshlrev_b32_e32 v94, 16, v96
	v_and_b32_e32 v95, 0xffff0000, v96
	v_lshlrev_b32_e32 v96, 16, v97
	v_and_b32_e32 v97, 0xffff0000, v97
	s_waitcnt vmcnt(28)
	v_lshlrev_b32_e32 v98, 16, v100
	v_and_b32_e32 v99, 0xffff0000, v100
	v_lshlrev_b32_e32 v100, 16, v101
	v_and_b32_e32 v101, 0xffff0000, v101
	s_waitcnt vmcnt(27)
	v_lshlrev_b32_e32 v102, 16, v104
	v_and_b32_e32 v103, 0xffff0000, v104
	v_lshlrev_b32_e32 v104, 16, v105
	v_and_b32_e32 v105, 0xffff0000, v105
	s_waitcnt vmcnt(26)
	v_lshlrev_b32_e32 v106, 16, v108
	v_and_b32_e32 v107, 0xffff0000, v108
	v_lshlrev_b32_e32 v108, 16, v109
	v_and_b32_e32 v109, 0xffff0000, v109
	s_waitcnt vmcnt(25)
	v_lshlrev_b32_e32 v110, 16, v112
	v_and_b32_e32 v111, 0xffff0000, v112
	v_lshlrev_b32_e32 v112, 16, v113
	v_and_b32_e32 v113, 0xffff0000, v113
	s_waitcnt vmcnt(24)
	v_lshlrev_b32_e32 v114, 16, v116
	v_and_b32_e32 v115, 0xffff0000, v116
	v_lshlrev_b32_e32 v116, 16, v117
	v_and_b32_e32 v117, 0xffff0000, v117
	v_mul_f32_e32 v245, 0x3fb8aa3b, v244
	v_fma_f32 v246, v244, s94, -v245
	v_rndne_f32_e32 v247, v245
	v_fmac_f32_e32 v246, 0x32a5705f, v244
	v_sub_f32_e32 v245, v245, v247
	v_add_f32_e32 v245, v245, v246
	v_exp_f32_e32 v245, v245
	v_cvt_i32_f32_e32 v246, v247
	v_cmp_ngt_f32_e32 vcc, 0xc2ce8ed0, v244
	v_ldexp_f32 v245, v245, v246
	s_nop 0
	v_cndmask_b32_e32 v245, 0, v245, vcc
	v_cmp_nlt_f32_e32 vcc, 0x42b17218, v244
	s_nop 1
	v_cndmask_b32_e32 v64, v204, v245, vcc
	v_mul_f32_e32 v245, 0xc2800000, v64
	v_mul_f32_e32 v245, 0x3fb8aa3b, v245
	v_exp_f32_e32 v84, v245
	s_nop 0
	v_mov_b32_e32 v118, v84
	v_mov_b32_e32 v119, v84
	v_mul_f32_e64 v8, v147, -v64
	v_mul_f32_e32 v8, 0x3fb8aa3b, v8
	v_exp_f32_e32 v183, v8
	v_mul_f32_e64 v8, v149, -v64
	v_mul_f32_e32 v8, 0x3fb8aa3b, v8
	v_exp_f32_e32 v184, v8
	v_mul_f32_e64 v8, v150, -v64
	v_mul_f32_e32 v8, 0x3fb8aa3b, v8
	v_exp_f32_e32 v185, v8
	v_mul_f32_e64 v8, v151, -v64
	v_mul_f32_e32 v8, 0x3fb8aa3b, v8
	v_exp_f32_e32 v186, v8
	v_mul_f32_e64 v8, v152, -v64
	v_mul_f32_e32 v8, 0x3fb8aa3b, v8
	v_exp_f32_e32 v187, v8
	v_mul_f32_e64 v8, v153, -v64
	v_mul_f32_e32 v8, 0x3fb8aa3b, v8
	v_exp_f32_e32 v188, v8
	v_mul_f32_e64 v8, v154, -v64
	v_mul_f32_e32 v8, 0x3fb8aa3b, v8
	v_exp_f32_e32 v189, v8
	v_mul_f32_e64 v8, v155, -v64
	v_mul_f32_e32 v8, 0x3fb8aa3b, v8
	v_exp_f32_e32 v190, v8
	s_cmp_lg_u32 s43, 1
	s_mov_b32 s42, 6
	s_cselect_b64 s[54:55], -1, 0
	v_readlane_b32 s43, v241, 53
	s_branch .LBB0_704
